# K fragments of next block requested before barrier1 and ahead of last 16 attn stores; hand-written tail+head
# speedup vs baseline: 1.0223x; 1.0223x over previous
.LBB1_12:
	s_ashr_i32 s0, s2, 2
	s_and_b32 s27, s2, 7
	s_and_b32 s28, s0, -2
	s_lshl_b32 s1, s28, 11
	s_lshl_b32 s12, s27, 17
	s_add_i32 s1, s1, s12
	v_lshlrev_b32_e32 v6, 2, v0
	v_or_b32_e32 v2, s1, v6
	v_lshlrev_b32_e32 v2, 2, v2
	global_load_dwordx4 v[2:5], v2, s[4:5]
	s_lshr_b32 s22, s19, 6
	s_lshl_b32 s29, s22, 3
	s_lshl_b32 s13, s0, 11
	s_add_i32 s0, s29, s0
	s_and_b32 s0, s0, 62
	v_and_b32_e32 v42, 63, v0
	s_lshl_b32 s14, s27, 18
	s_lshl_b32 s0, s0, 12
	v_lshrrev_b32_e32 v43, 4, v0
	v_lshlrev_b32_e32 v230, 4, v0
	v_lshlrev_b32_e32 v231, 4, v42
	s_or_b32 s0, s14, s0
	v_mov_b32_e32 v39, 0
	v_mul_u32_u24_e32 v7, 0x44, v43
	v_and_b32_e32 v44, 0xf0, v230
	s_bitset1_b32 s13, 11
	v_or_b32_e32 v6, s12, v6
	v_or_b32_e32 v38, s0, v231
	s_movk_i32 s1, 0x1000
	v_lshl_add_u32 v45, v7, 2, v44
	v_add_lshl_u32 v46, v6, s13, 2
	v_lshl_add_u64 v[6:7], s[6:7], 0, v[38:39]
	v_add_u32_e32 v232, 0x24200, v45
	v_add_co_u32_e32 v40, vcc, s1, v6
	v_max_f32_e64 v35, |v35|, |v35|
	s_nop 0
	v_addc_co_u32_e32 v41, vcc, 0, v7, vcc
	v_max_f32_e64 v1, |v1|, |v1|
	v_max_f32_e32 v1, v1, v35
	s_brev_b32 s12, -2
	v_mov_b32_e32 v39, s3
	v_bfi_b32 v37, s12, v37, v39
	s_mov_b32 s12, 0
	v_readfirstlane_b32 s18, v37
	v_and_b32_e32 v35, 31, v0
	s_waitcnt vmcnt(0)
	ds_write_b128 v232, v[2:5]
	s_waitcnt lgkmcnt(0)
	s_barrier
	global_load_dwordx4 v[128:131], v46, s[4:5]
	v_div_scale_f32 v40, s[0:1], v1, v1, v36
	v_rcp_f32_e32 v41, v40
	v_bfe_u32 v38, v0, 5, 1
	v_fma_f32 v37, -v40, v41, 1.0
	v_fmac_f32_e32 v41, v37, v41
	v_div_scale_f32 v37, vcc, v36, v1, v36
	v_mul_f32_e32 v39, v37, v41
	v_fma_f32 v46, -v40, v39, v37
	v_fmac_f32_e32 v39, v46, v41
	v_fma_f32 v37, -v40, v39, v37
	v_div_fmas_f32 v37, v37, v41, v39
	v_div_scale_f32 v39, s[0:1], v1, v1, v34
	v_rcp_f32_e32 v40, v39
	v_div_fixup_f32 v36, v37, v1, v36
	v_cmp_lt_f32_e64 s[0:1], 0, v1
	v_fma_f32 v37, -v39, v40, 1.0
	v_fmac_f32_e32 v40, v37, v40
	v_div_scale_f32 v37, vcc, v34, v1, v34
	v_mul_f32_e32 v41, v37, v40
	v_fma_f32 v46, -v39, v41, v37
	v_fmac_f32_e32 v41, v46, v40
	v_fma_f32 v37, -v39, v41, v37
	v_div_fmas_f32 v37, v37, v40, v41
	v_div_fixup_f32 v34, v37, v1, v34
	v_cndmask_b32_e64 v36, 0, v36, s[0:1]
	v_cndmask_b32_e64 v34, 0, v34, s[0:1]
	s_lshl_b32 s0, s2, 16
	s_and_b32 s1, s19, 0xffffffc0
	v_bfe_u32 v37, v0, 2, 1
	v_and_b32_e32 v39, 3, v0
	v_lshrrev_b32_e32 v40, 1, v0
	v_readfirstlane_b32 s30, v36
	s_add_i32 s0, s1, s0
	v_and_or_b32 v39, v40, 12, v39
	v_cmp_eq_u32_e32 vcc, v37, v38
	s_mov_b32 s14, s12
	s_mov_b32 s15, s12
	s_mov_b32 s13, s12
	v_mov_b64_e32 v[48:49], s[14:15]
	v_mov_b32_e32 v36, s0
	v_mov_b64_e32 v[46:47], s[12:13]
	v_readfirstlane_b32 s14, v1
	v_readfirstlane_b32 s13, v34
	v_cndmask_b32_e32 v233, 16, v39, vcc
	v_mbcnt_lo_u32_b32 v34, -1, 0
	v_mbcnt_hi_u32_b32 v34, -1, v34
	v_and_b32_e32 v40, 64, v34
	v_xor_b32_e32 v39, 32, v34
	v_add_u32_e32 v40, 64, v40
	v_cmp_lt_i32_e32 vcc, v39, v40
	s_cmp_lt_u32 s19, 64
	v_mul_u32_u24_e32 v1, 0x44, v35
	v_cndmask_b32_e32 v34, v34, v39, vcc
	v_lshlrev_b32_e32 v234, 2, v34
	v_lshlrev_b32_e32 v34, 2, v35
	s_cselect_b64 s[2:3], -1, 0
	s_cmp_gt_u32 s19, 63
	s_mul_i32 s19, s22, 0x2200
	v_lshlrev_b32_e32 v1, 2, v1
	v_or_b32_e32 v235, 0x26400, v34
	v_or_b32_e32 v236, 0x26800, v34
	s_cselect_b64 s[20:21], -1, 0
	v_lshlrev_b32_e32 v34, 4, v38
	s_lshl_b32 s15, s22, 15
	s_add_i32 s19, s19, 0x13200
	v_add_u32_e32 v36, 0x24200, v1
	v_and_b32_e32 v37, 32, v0
	v_add_u32_e32 v39, 0x11000, v1
	s_or_b32 s33, s15, 0x2000
	s_or_b32 s34, s15, 0x3000
	s_or_b32 s35, s15, 0x4000
	s_or_b32 s36, s15, 0x5000
	s_or_b32 s37, s15, 0x6000
	s_or_b32 s38, s15, 0x7000
	v_lshl_or_b32 v35, s22, 5, v35
	s_movk_i32 s15, 0x110
	v_add3_u32 v238, s19, v1, v34
	v_bfe_u32 v239, v0, 4, 2
	v_and_b32_e32 v1, 15, v0
	v_mov_b32_e32 v38, s19
	v_bfe_u32 v0, v0, 3, 1
	v_mad_u64_u32 v[164:165], s[24:25], v35, s15, v[34:35]
	v_lshlrev_b32_e32 v35, 2, v43
	v_mad_u32_u24 v38, v239, s15, v38
	v_lshlrev_b32_e32 v1, 4, v1
	v_or_b32_e32 v241, s29, v0
	v_mul_u32_u24_e32 v0, 0x110, v43
	v_cmp_gt_u32_e64 s[0:1], 32, v42
	s_lshl_b32 s31, s22, 7
	v_or_b32_e32 v165, 0x26400, v35
	v_add_u32_e32 v237, 0x11000, v45
	s_add_i32 s39, s29, s28
	v_and_b32_e32 v240, 0x70, v230
	v_or_b32_e32 v242, 0x26800, v35
	s_mov_b32 s19, s18
	s_mov_b32 s15, s14
	s_mov_b32 s40, s30
	s_mov_b32 s41, s30
	s_mov_b32 s42, s30
	s_mov_b32 s43, s30
	s_mov_b32 s44, s30
	s_mov_b32 s45, s30
	s_mov_b32 s46, s30
	s_mov_b32 s47, s13
	s_mov_b32 s48, s13
	s_mov_b32 s49, s13
	s_mov_b32 s50, s13
	s_mov_b32 s51, s13
	s_mov_b32 s52, s13
	s_mov_b32 s53, s13
	v_add_u32_e32 v243, v36, v37
	s_mov_b32 s22, 0x3e38aa3b
	v_add_u32_e32 v244, v39, v34
	v_add_u32_e32 v245, v44, v0
	s_movk_i32 s54, 0x1f80
	v_add_u32_e32 v246, v38, v1
	s_mov_b32 s57, s12
	s_add_i32 s62, s28, s29
	s_lshl_b32 s62, s62, 12
	s_lshl_b32 s66, s27, 18
	s_and_b32 s63, s62, 0x3f000
	s_or_b32 s63, s63, s66
	v_or_b32_e32 v2, s63, v231
	global_load_dwordx4 v[48:51], v2, s[6:7]
	global_load_dwordx4 v[52:55], v2, s[6:7] offset:1024
	global_load_dwordx4 v[56:59], v2, s[6:7] offset:2048
	global_load_dwordx4 v[60:63], v2, s[6:7] offset:3072
	s_add_i32 s63, s62, 0x4000
	s_and_b32 s63, s63, 0x3f000
	s_or_b32 s63, s63, s66
	v_or_b32_e32 v3, s63, v231
	global_load_dwordx4 v[40:43], v3, s[6:7] offset:2048
	global_load_dwordx4 v[44:47], v3, s[6:7] offset:3072
	s_add_i32 s63, s62, 0x6000
	s_and_b32 s63, s63, 0x3f000
	s_or_b32 s63, s63, s66
	v_or_b32_e32 v2, s63, v231
	global_load_dwordx4 v[148:151], v2, s[6:7] offset:3072
	s_add_i32 s63, s62, 0x7000
	s_and_b32 s63, s63, 0x3f000
	s_or_b32 s63, s63, s66
	v_or_b32_e32 v3, s63, v231
	global_load_dwordx4 v[132:135], v3, s[6:7]
	global_load_dwordx4 v[136:139], v3, s[6:7] offset:1024
	global_load_dwordx4 v[140:143], v3, s[6:7] offset:2048
	global_load_dwordx4 v[144:147], v3, s[6:7] offset:3072
	s_add_i32 s63, s62, 0x1000
	s_and_b32 s63, s63, 0x3f000
	s_or_b32 s63, s63, s66
	v_or_b32_e32 v2, s63, v231
	global_load_dwordx4 v[152:155], v2, s[6:7]
	global_load_dwordx4 v[156:159], v2, s[6:7] offset:1024
	s_add_i32 s63, s62, 0x4000
	s_and_b32 s63, s63, 0x3f000
	s_or_b32 s63, s63, s66
	v_or_b32_e32 v3, s63, v231
	global_load_dwordx4 v[32:35], v3, s[6:7]
	global_load_dwordx4 v[36:39], v3, s[6:7] offset:1024
	s_add_i32 s63, s62, 0x5000
	s_and_b32 s63, s63, 0x3f000
	s_or_b32 s63, s63, s66
	v_or_b32_e32 v2, s63, v231
	global_load_dwordx4 v[16:19], v2, s[6:7]
	global_load_dwordx4 v[20:23], v2, s[6:7] offset:1024
	global_load_dwordx4 v[24:27], v2, s[6:7] offset:2048
	global_load_dwordx4 v[28:31], v2, s[6:7] offset:3072
	s_add_i32 s63, s62, 0x6000
	s_and_b32 s63, s63, 0x3f000
	s_or_b32 s63, s63, s66
	v_or_b32_e32 v3, s63, v231
	global_load_dwordx4 v[4:7], v3, s[6:7]
	global_load_dwordx4 v[8:11], v3, s[6:7] offset:1024
	global_load_dwordx4 v[12:15], v3, s[6:7] offset:2048
	s_add_i32 s63, s62, 0x3000
	s_and_b32 s63, s63, 0x3f000
	s_or_b32 s63, s63, s66
	v_or_b32_e32 v2, s63, v231
	global_load_dwordx4 v[80:83], v2, s[6:7]
	global_load_dwordx4 v[84:87], v2, s[6:7] offset:1024
	global_load_dwordx4 v[88:91], v2, s[6:7] offset:2048
	global_load_dwordx4 v[92:95], v2, s[6:7] offset:3072
	s_add_i32 s63, s62, 0x2000
	s_and_b32 s63, s63, 0x3f000
	s_or_b32 s63, s63, s66
	v_or_b32_e32 v3, s63, v231
	global_load_dwordx4 v[96:99], v3, s[6:7]
	global_load_dwordx4 v[100:103], v3, s[6:7] offset:1024
	global_load_dwordx4 v[108:111], v3, s[6:7] offset:2048
	global_load_dwordx4 v[192:195], v3, s[6:7] offset:3072
	s_add_i32 s63, s62, 0x1000
	s_and_b32 s63, s63, 0x3f000
	s_or_b32 s63, s63, s66
	v_or_b32_e32 v2, s63, v231
	global_load_dwordx4 v[174:177], v2, s[6:7] offset:2048
	global_load_dwordx4 v[178:181], v2, s[6:7] offset:3072
	s_waitcnt vmcnt(0)
	s_branch .LBB1_14
.LBB1_13:
	s_waitcnt vmcnt(12)
	v_cvt_pk_f16_f32 v151, v120, v121
	v_cvt_pk_f16_f32 v150, v100, v101
	v_cvt_pk_f16_f32 v149, v98, v99
	v_cvt_pk_f16_f32 v148, v112, v113
	s_add_i32 s24, s57, 1
	s_cmp_lg_u32 s57, 7
	s_waitcnt vmcnt(11)
	v_mfma_f32_32x32x16_f16 v[0:15], v[144:147], v[148:151], v[0:15]
	s_cselect_b32 s59, s24, 7
	s_lshl_b32 s25, s59, 2
	s_and_b32 s25, s25, 56
	s_or_b32 s58, s25, s27
	s_lshl_b32 s25, s55, 5
	s_and_b32 s59, s59, 1
	s_waitcnt vmcnt(10)
	v_mfma_f32_32x32x16_f16 v[16:31], v[140:143], v[148:151], v[16:31]
	v_cvt_pk_f16_f32 v143, v180, v181
	v_cvt_pk_f16_f32 v142, v124, v125
	v_cvt_pk_f16_f32 v141, v122, v123
	v_cvt_pk_f16_f32 v140, v102, v103
	s_waitcnt vmcnt(9)
	s_nop 0
	v_mfma_f32_32x32x16_f16 v[0:15], v[136:139], v[140:143], v[0:15]
	s_waitcnt vmcnt(8)
	v_mfma_f32_32x32x16_f16 v[16:31], v[132:135], v[140:143], v[16:31]
	s_add_i32 s61, s35, s60
	s_and_b32 s61, s61, 0x3f000
	v_or_b32_e32 v144, s61, v248
	s_add_i32 s61, s36, s60
	s_and_b32 s61, s61, 0x3f000
	v_or_b32_e32 v160, s61, v248
	global_load_dwordx4 v[132:135], v144, s[16:17]
	global_load_dwordx4 v[136:139], v144, s[16:17] offset:1024
	global_load_dwordx4 v[140:143], v144, s[16:17] offset:2048
	s_nop 0
	global_load_dwordx4 v[144:147], v144, s[16:17] offset:3072
	s_nop 0
	global_load_dwordx4 v[148:151], v160, s[16:17]
	global_load_dwordx4 v[152:155], v160, s[16:17] offset:1024
	global_load_dwordx4 v[156:159], v160, s[16:17] offset:2048
	s_nop 0
	global_load_dwordx4 v[160:163], v160, s[16:17] offset:3072
	v_cvt_pk_f16_f32 v253, v96, v97
	v_cvt_pk_f16_f32 v252, v84, v85
	v_cvt_pk_f16_f32 v251, v82, v83
	v_cvt_pk_f16_f32 v250, v80, v81
	s_waitcnt vmcnt(15)
	s_nop 0
	v_mfma_f32_32x32x16_f16 v[0:15], v[60:63], v[250:253], v[0:15]
	s_waitcnt vmcnt(14)
	v_mfma_f32_32x32x16_f16 v[16:31], v[56:59], v[250:253], v[16:31]
	v_cvt_pk_f16_f32 v59, v94, v95
	v_cvt_pk_f16_f32 v58, v90, v91
	v_cvt_pk_f16_f32 v57, v88, v89
	v_cvt_pk_f16_f32 v56, v86, v87
	s_waitcnt vmcnt(13)
	s_nop 0
	v_mfma_f32_32x32x16_f16 v[0:15], v[52:55], v[56:59], v[0:15]
	s_waitcnt vmcnt(12)
	v_mfma_f32_32x32x16_f16 v[16:31], v[48:51], v[56:59], v[16:31]
	v_cvt_pk_f16_f32 v51, v176, v177
	v_cvt_pk_f16_f32 v50, v110, v111
	v_cvt_pk_f16_f32 v49, v108, v109
	v_cvt_pk_f16_f32 v48, v92, v93
	s_waitcnt vmcnt(11)
	s_nop 0
	v_mfma_f32_32x32x16_f16 v[0:15], v[44:47], v[48:51], v[0:15]
	s_waitcnt vmcnt(10)
	v_mfma_f32_32x32x16_f16 v[16:31], v[40:43], v[48:51], v[16:31]
	v_cvt_pk_f16_f32 v43, v206, v207
	v_cvt_pk_f16_f32 v42, v194, v195
	v_cvt_pk_f16_f32 v41, v192, v193
	v_cvt_pk_f16_f32 v40, v174, v175
	s_waitcnt vmcnt(9)
	s_nop 0
	v_mfma_f32_32x32x16_f16 v[0:15], v[36:39], v[40:43], v[0:15]
	s_waitcnt vmcnt(8)
	v_mfma_f32_32x32x16_f16 v[16:31], v[32:35], v[40:43], v[16:31]
	s_add_i32 s61, s37, s60
	s_add_i32 s60, s38, s60
	s_and_b32 s61, s61, 0x3f000
	s_and_b32 s60, s60, 0x3f000
	v_or_b32_e32 v44, s61, v248
	v_or_b32_e32 v60, s60, v248
	global_load_dwordx4 v[32:35], v44, s[16:17]
	global_load_dwordx4 v[36:39], v44, s[16:17] offset:1024
	global_load_dwordx4 v[40:43], v44, s[16:17] offset:2048
	s_nop 0
	global_load_dwordx4 v[44:47], v44, s[16:17] offset:3072
	s_nop 0
	global_load_dwordx4 v[48:51], v60, s[16:17]
	global_load_dwordx4 v[52:55], v60, s[16:17] offset:1024
	global_load_dwordx4 v[56:59], v60, s[16:17] offset:2048
	s_nop 0
	global_load_dwordx4 v[60:63], v60, s[16:17] offset:3072
	v_cvt_pk_f16_f32 v251, v74, v75
	v_cvt_pk_f16_f32 v250, v68, v69
	v_cvt_pk_f16_f32 v249, v66, v67
	v_cvt_pk_f16_f32 v248, v64, v65
	s_waitcnt vmcnt(15)
	s_nop 0
	v_mfma_f32_32x32x16_f16 v[0:15], v[132:135], v[248:251], v[0:15]
	v_cvt_pk_f16_f32 v135, v172, v173
	v_cvt_pk_f16_f32 v134, v106, v107
	v_cvt_pk_f16_f32 v133, v104, v105
	v_cvt_pk_f16_f32 v132, v72, v73
	s_waitcnt vmcnt(14)
	v_mfma_f32_32x32x16_f16 v[16:31], v[136:139], v[248:251], v[16:31]
	s_waitcnt vmcnt(13)
	v_mfma_f32_32x32x16_f16 v[0:15], v[140:143], v[132:135], v[0:15]
	s_waitcnt vmcnt(12)
	v_mfma_f32_32x32x16_f16 v[16:31], v[144:147], v[132:135], v[16:31]
	v_cvt_pk_f16_f32 v135, v202, v203
	v_cvt_pk_f16_f32 v134, v190, v191
	v_cvt_pk_f16_f32 v133, v188, v189
	v_cvt_pk_f16_f32 v132, v170, v171
	s_waitcnt vmcnt(11)
	s_nop 0
	v_mfma_f32_32x32x16_f16 v[0:15], v[148:151], v[132:135], v[0:15]
	s_waitcnt vmcnt(10)
	v_mfma_f32_32x32x16_f16 v[16:31], v[152:155], v[132:135], v[16:31]
	v_cvt_pk_f16_f32 v135, v222, v223
	v_cvt_pk_f16_f32 v134, v216, v217
	v_cvt_pk_f16_f32 v133, v214, v215
	v_cvt_pk_f16_f32 v132, v200, v201
	s_waitcnt vmcnt(9)
	s_nop 0
	v_mfma_f32_32x32x16_f16 v[0:15], v[156:159], v[132:135], v[0:15]
	s_waitcnt vmcnt(8)
	v_mfma_f32_32x32x16_f16 v[16:31], v[160:163], v[132:135], v[16:31]
	v_cvt_pk_f16_f32 v135, v168, v169
	v_cvt_pk_f16_f32 v134, v78, v79
	v_cvt_pk_f16_f32 v133, v76, v77
	v_cvt_pk_f16_f32 v132, v70, v71
	s_waitcnt vmcnt(7)
	s_nop 0
	v_mfma_f32_32x32x16_f16 v[0:15], v[32:35], v[132:135], v[0:15]
	v_cvt_pk_f16_f32 v35, v198, v199
	v_cvt_pk_f16_f32 v34, v186, v187
	v_cvt_pk_f16_f32 v33, v184, v185
	v_cvt_pk_f16_f32 v32, v126, v127
	s_waitcnt vmcnt(6)
	v_mfma_f32_32x32x16_f16 v[16:31], v[36:39], v[132:135], v[16:31]
	s_waitcnt vmcnt(5)
	v_mfma_f32_32x32x16_f16 v[0:15], v[40:43], v[32:35], v[0:15]
	s_waitcnt vmcnt(4)
	v_mfma_f32_32x32x16_f16 v[16:31], v[44:47], v[32:35], v[16:31]
	v_cvt_pk_f16_f32 v35, v220, v221
	v_cvt_pk_f16_f32 v34, v212, v213
	v_cvt_pk_f16_f32 v33, v210, v211
	v_cvt_pk_f16_f32 v32, v196, v197
	s_waitcnt vmcnt(3)
	s_nop 0
	v_mfma_f32_32x32x16_f16 v[0:15], v[48:51], v[32:35], v[0:15]
	s_waitcnt vmcnt(2)
	v_mfma_f32_32x32x16_f16 v[16:31], v[52:55], v[32:35], v[16:31]
	v_cvt_pk_f16_f32 v35, v228, v229
	v_cvt_pk_f16_f32 v34, v226, v227
	v_cvt_pk_f16_f32 v33, v224, v225
	v_cvt_pk_f16_f32 v32, v218, v219
	s_waitcnt vmcnt(1)
	s_nop 0
	v_mfma_f32_32x32x16_f16 v[0:15], v[56:59], v[32:35], v[0:15]
	s_waitcnt vmcnt(0)
	v_mfma_f32_32x32x16_f16 v[16:31], v[60:63], v[32:35], v[16:31]
	s_or_b32 s62, s39, s59
	s_lshl_b32 s62, s62, 12
	s_lshl_b32 s66, s58, 18
	s_and_b32 s63, s62, 0x3f000
	s_or_b32 s63, s63, s66
	v_or_b32_e32 v252, s63, v231
	global_load_dwordx4 v[48:51], v252, s[6:7]
	global_load_dwordx4 v[52:55], v252, s[6:7] offset:1024
	global_load_dwordx4 v[56:59], v252, s[6:7] offset:2048
	global_load_dwordx4 v[60:63], v252, s[6:7] offset:3072
	s_add_i32 s63, s62, 0x4000
	s_and_b32 s63, s63, 0x3f000
	s_or_b32 s63, s63, s66
	v_or_b32_e32 v253, s63, v231
	global_load_dwordx4 v[40:43], v253, s[6:7] offset:2048
	global_load_dwordx4 v[44:47], v253, s[6:7] offset:3072
	s_add_i32 s63, s62, 0x6000
	s_and_b32 s63, s63, 0x3f000
	s_or_b32 s63, s63, s66
	v_or_b32_e32 v252, s63, v231
	global_load_dwordx4 v[148:151], v252, s[6:7] offset:3072
	s_add_i32 s63, s62, 0x7000
	s_and_b32 s63, s63, 0x3f000
	s_or_b32 s63, s63, s66
	v_or_b32_e32 v253, s63, v231
	global_load_dwordx4 v[132:135], v253, s[6:7]
	global_load_dwordx4 v[136:139], v253, s[6:7] offset:1024
	global_load_dwordx4 v[140:143], v253, s[6:7] offset:2048
	global_load_dwordx4 v[144:147], v253, s[6:7] offset:3072
	s_add_i32 s63, s62, 0x1000
	s_and_b32 s63, s63, 0x3f000
	s_or_b32 s63, s63, s66
	v_or_b32_e32 v252, s63, v231
	global_load_dwordx4 v[152:155], v252, s[6:7]
	global_load_dwordx4 v[156:159], v252, s[6:7] offset:1024
	s_nop 9
	v_mul_f32_e64 v0, s18, v0
	v_mul_f32_e64 v1, s19, v1
	v_mul_f32_e64 v2, s18, v2
	v_mul_f32_e64 v3, s19, v3
	v_pk_mul_f32 v[16:17], s[18:19], v[16:17]
	v_pk_mul_f32 v[18:19], s[18:19], v[18:19]
	ds_write_b128 v164, v[0:3]
	ds_write_b128 v164, v[16:19] offset:128
	v_pk_mul_f32 v[0:1], s[18:19], v[4:5]
	v_pk_mul_f32 v[2:3], s[18:19], v[6:7]
	v_pk_mul_f32 v[4:5], s[18:19], v[20:21]
	v_pk_mul_f32 v[6:7], s[18:19], v[22:23]
	ds_write_b128 v164, v[0:3] offset:32
	ds_write_b128 v164, v[4:7] offset:160
	v_pk_mul_f32 v[0:1], s[18:19], v[8:9]
	v_pk_mul_f32 v[2:3], s[18:19], v[10:11]
	v_pk_mul_f32 v[4:5], s[18:19], v[24:25]
	v_pk_mul_f32 v[6:7], s[18:19], v[26:27]
	ds_write_b128 v164, v[0:3] offset:64
	ds_write_b128 v164, v[4:7] offset:192
	v_pk_mul_f32 v[0:1], s[18:19], v[12:13]
	v_pk_mul_f32 v[2:3], s[18:19], v[14:15]
	v_pk_mul_f32 v[4:5], s[18:19], v[28:29]
	v_pk_mul_f32 v[6:7], s[18:19], v[30:31]
	ds_write_b128 v164, v[0:3] offset:96
	ds_write_b128 v164, v[4:7] offset:224
	s_waitcnt lgkmcnt(0)
	s_barrier
	ds_read2_b32 v[0:1], v235 offset1:32
	ds_read2_b32 v[2:3], v235 offset0:64 offset1:96
	ds_read2_b32 v[4:5], v235 offset0:128 offset1:160
	ds_read2_b32 v[6:7], v235 offset0:192 offset1:224
	ds_read2_b32 v[10:11], v236 offset0:128 offset1:160
	ds_read2_b32 v[16:17], v165 offset1:32
	ds_write_b128 v232, v[128:131]
	s_waitcnt lgkmcnt(6)
	v_max_f32_e32 v8, v1, v1
	v_max_f32_e32 v9, v0, v0
	v_max_f32_e32 v8, v9, v8
	s_waitcnt lgkmcnt(5)
	v_max3_f32 v8, v8, v2, v3
	s_waitcnt lgkmcnt(4)
	v_max3_f32 v8, v8, v4, v5
	s_waitcnt lgkmcnt(3)
	v_max3_f32 v14, v8, v6, v7
	ds_read2_b32 v[8:9], v236 offset1:32
	v_sub_f32_e32 v0, v0, v14
	v_sub_f32_e32 v1, v1, v14
	v_exp_f32_e32 v0, v0
	v_exp_f32_e32 v1, v1
	v_sub_f32_e32 v4, v4, v14
	v_sub_f32_e32 v5, v5, v14
	v_exp_f32_e32 v4, v4
	v_exp_f32_e32 v5, v5
	s_waitcnt lgkmcnt(0)
	v_pk_mul_f32 v[0:1], v[8:9], v[0:1]
	ds_read2_b32 v[8:9], v236 offset0:64 offset1:96
	v_sub_f32_e32 v2, v2, v14
	v_sub_f32_e32 v3, v3, v14
	v_exp_f32_e32 v2, v2
	v_exp_f32_e32 v3, v3
	ds_read2_b32 v[12:13], v236 offset0:192 offset1:224
	v_sub_f32_e32 v6, v6, v14
	v_sub_f32_e32 v7, v7, v14
	v_pk_mul_f32 v[18:19], v[10:11], v[4:5]
	v_sub_f32_e32 v4, v247, v14
	ds_read2_b32 v[22:23], v165 offset0:64 offset1:96
	ds_read2_b32 v[24:25], v165 offset0:128 offset1:160
	ds_read2_b32 v[26:27], v165 offset0:192 offset1:224
	v_exp_f32_e32 v6, v6
	v_exp_f32_e32 v7, v7
	v_exp_f32_e32 v34, v4
	v_max_f32_e32 v4, v17, v17
	v_max_f32_e32 v5, v16, v16
	v_add_f32_e32 v0, 0, v0
	s_waitcnt lgkmcnt(4)
	v_pk_mul_f32 v[2:3], v[8:9], v[2:3]
	v_max_f32_e32 v4, v5, v4
	v_add_f32_e32 v0, v0, v1
	s_waitcnt lgkmcnt(2)
	v_max3_f32 v4, v4, v22, v23
	v_add_f32_e32 v0, v0, v2
	s_waitcnt lgkmcnt(1)
	v_max3_f32 v4, v4, v24, v25
	v_add_f32_e32 v0, v0, v3
	v_pk_mul_f32 v[20:21], v[12:13], v[6:7]
	s_waitcnt lgkmcnt(0)
	v_max3_f32 v35, v4, v26, v27
	v_add_f32_e32 v18, v0, v18
	ds_read_b128 v[0:3], v245
	ds_read_b128 v[4:7], v237
	v_sub_f32_e32 v8, v16, v35
	v_exp_f32_e32 v16, v8
	ds_read2_b32 v[28:29], v242 offset1:32
	ds_read_b128 v[8:11], v245 offset:34816
	ds_read_b128 v[12:15], v245 offset:60928
	s_min_u32 s57, s57, 5
	s_waitcnt lgkmcnt(3)
	v_pk_add_f32 v[0:1], v[0:1], v[4:5]
	v_pk_add_f32 v[2:3], v[2:3], v[6:7]
	v_pk_fma_f32 v[30:31], v[16:17], v[0:1], 0 op_sel_hi:[0,1,0]
	v_sub_f32_e32 v0, v17, v35
	v_pk_fma_f32 v[32:33], v[16:17], v[2:3], 0 op_sel_hi:[0,1,0]
	v_exp_f32_e32 v17, v0
	v_add_f32_e32 v0, v18, v19
	v_add_f32_e32 v0, v0, v20
	v_add_f32_e32 v36, v0, v21
	ds_read_b128 v[0:3], v245 offset:8704
	ds_read_b128 v[4:7], v245 offset:17408
	s_waitcnt lgkmcnt(4)
	v_pk_mul_f32 v[18:19], v[28:29], v[16:17]
	v_sub_f32_e32 v16, v22, v35
	v_exp_f32_e32 v16, v16
	v_add_f32_e32 v20, 0, v18
	v_mov_b32_e32 v18, v17
	s_waitcnt lgkmcnt(1)
	v_pk_fma_f32 v[0:1], v[18:19], v[0:1], v[30:31] op_sel_hi:[0,1,1]
	v_pk_fma_f32 v[2:3], v[18:19], v[2:3], v[32:33] op_sel_hi:[0,1,1]
	s_waitcnt lgkmcnt(0)
	v_pk_fma_f32 v[4:5], v[16:17], v[4:5], v[0:1] op_sel_hi:[0,1,1]
	v_sub_f32_e32 v0, v23, v35
	v_pk_fma_f32 v[6:7], v[16:17], v[6:7], v[2:3] op_sel_hi:[0,1,1]
	v_exp_f32_e32 v17, v0
	v_add_f32_e32 v21, v20, v19
	ds_read_b128 v[0:3], v245 offset:26112
	ds_read2_b32 v[18:19], v242 offset0:64 offset1:96
	v_sub_f32_e32 v22, v24, v35
	v_exp_f32_e32 v22, v22
	v_mov_b32_e32 v20, v17
	s_waitcnt lgkmcnt(1)
	v_pk_fma_f32 v[0:1], v[20:21], v[0:1], v[4:5] op_sel_hi:[0,1,1]
	v_pk_fma_f32 v[2:3], v[20:21], v[2:3], v[6:7] op_sel_hi:[0,1,1]
	ds_read2_b32 v[4:5], v242 offset0:128 offset1:160
	v_pk_fma_f32 v[8:9], v[22:23], v[8:9], v[0:1] op_sel_hi:[0,1,1]
	v_sub_f32_e32 v0, v25, v35
	v_pk_fma_f32 v[10:11], v[22:23], v[10:11], v[2:3] op_sel_hi:[0,1,1]
	v_exp_f32_e32 v23, v0
	s_waitcnt lgkmcnt(1)
	v_pk_mul_f32 v[0:1], v[18:19], v[16:17]
	s_lshl_b32 s58, s58, 18
	v_add_f32_e32 v0, v21, v0
	v_add_f32_e32 v2, v0, v1
	s_waitcnt lgkmcnt(0)
	v_pk_mul_f32 v[0:1], v[4:5], v[22:23]
	v_sub_f32_e32 v4, v26, v35
	v_add_f32_e32 v0, v2, v0
	v_add_f32_e32 v17, v0, v1
	ds_read_b128 v[0:3], v245 offset:43520
	v_exp_f32_e32 v18, v4
	ds_read2_b32 v[20:21], v242 offset0:192 offset1:224
	v_sub_f32_e32 v4, v27, v35
	v_exp_f32_e32 v19, v4
	ds_read_b128 v[4:7], v245 offset:52224
	v_mov_b32_e32 v16, v23
	s_waitcnt lgkmcnt(2)
	v_pk_fma_f32 v[0:1], v[16:17], v[0:1], v[8:9] op_sel_hi:[0,1,1]
	s_waitcnt lgkmcnt(1)
	v_pk_mul_f32 v[8:9], v[20:21], v[18:19]
	v_pk_fma_f32 v[2:3], v[16:17], v[2:3], v[10:11] op_sel_hi:[0,1,1]
	v_add_f32_e32 v8, v17, v8
	v_add_f32_e32 v8, v8, v9
	s_waitcnt lgkmcnt(0)
	v_pk_fma_f32 v[0:1], v[18:19], v[4:5], v[0:1] op_sel_hi:[0,1,1]
	v_div_scale_f32 v5, s[60:61], v8, v8, 1.0
	v_pk_fma_f32 v[2:3], v[18:19], v[6:7], v[2:3] op_sel_hi:[0,1,1]
	v_rcp_f32_e32 v6, v5
	v_mov_b32_e32 v4, v19
	v_pk_fma_f32 v[2:3], v[4:5], v[14:15], v[2:3] op_sel_hi:[0,1,1]
	v_pk_fma_f32 v[0:1], v[4:5], v[12:13], v[0:1] op_sel_hi:[0,1,1]
	v_fma_f32 v4, -v5, v6, 1.0
	v_fmac_f32_e32 v6, v4, v6
	v_div_scale_f32 v4, vcc, 1.0, v8, 1.0
	v_mul_f32_e32 v7, v4, v6
	v_fma_f32 v9, -v5, v7, v4
	v_fmac_f32_e32 v7, v9, v6
	v_fma_f32 v4, -v5, v7, v4
	v_div_fmas_f32 v4, v4, v6, v7
	s_lshl_b32 s60, s56, 19
	s_lshl_b32 s61, s55, 13
	v_div_fixup_f32 v4, v4, v8, 1.0
	s_add_i32 s60, s60, s61
	v_pk_mul_f32 v[2:3], v[2:3], v[4:5] op_sel_hi:[1,0]
	v_pk_mul_f32 v[0:1], v[0:1], v[4:5] op_sel_hi:[1,0]
	v_or_b32_e32 v4, s60, v230
	s_lshl_b32 s60, s57, 2
	s_add_i32 s60, s60, 8
	s_and_b32 s60, s60, 56
	s_and_b32 s57, s57, 1
	s_or_b32 s60, s60, s27
	s_or_b32 s57, s57, s28
	s_lshl_b32 s60, s60, 19
	s_lshl_b32 s57, s57, 13
	s_add_i32 s60, s60, s57
	s_or_b32 s62, s39, s59
	s_lshl_b32 s62, s62, 12
	global_store_dwordx4 v4, v[0:3], s[8:9] nt
	v_mov_b32_e32 v252, v34
	v_mov_b32_e32 v253, v36
	v_or_b32_e32 v0, s60, v230
	s_barrier
	global_load_dwordx4 v[128:131], v0, s[4:5]
	s_add_i32 s63, s62, 0x4000
	s_and_b32 s63, s63, 0x3f000
	s_or_b32 s63, s63, s58
	v_or_b32_e32 v2, s63, v231
	global_load_dwordx4 v[32:35], v2, s[6:7]
	global_load_dwordx4 v[36:39], v2, s[6:7] offset:1024
	s_add_i32 s63, s62, 0x5000
	s_and_b32 s63, s63, 0x3f000
	s_or_b32 s63, s63, s58
	v_or_b32_e32 v3, s63, v231
	global_load_dwordx4 v[16:19], v3, s[6:7]
	global_load_dwordx4 v[20:23], v3, s[6:7] offset:1024
	global_load_dwordx4 v[24:27], v3, s[6:7] offset:2048
	global_load_dwordx4 v[28:31], v3, s[6:7] offset:3072
	s_add_i32 s63, s62, 0x6000
	s_and_b32 s63, s63, 0x3f000
	s_or_b32 s63, s63, s58
	v_or_b32_e32 v2, s63, v231
	global_load_dwordx4 v[4:7], v2, s[6:7]
	global_load_dwordx4 v[8:11], v2, s[6:7] offset:1024
	global_load_dwordx4 v[12:15], v2, s[6:7] offset:2048
	v_div_scale_f32 v1, s[64:65], v253, v253, v252
	v_rcp_f32_e32 v2, v1
	s_nop 0
	v_fma_f32 v0, -v1, v2, 1.0
	v_fmac_f32_e32 v2, v0, v2
	v_div_scale_f32 v0, vcc, v252, v253, v252
	v_mul_f32_e32 v3, v0, v2
	v_fma_f32 v248, -v1, v3, v0
	v_fmac_f32_e32 v3, v248, v2
	v_fma_f32 v0, -v1, v3, v0
	v_div_fmas_f32 v0, v0, v2, v3
	v_div_fixup_f32 v1, v0, v253, v252
	v_mul_f32_e32 v0, s18, v1
	v_mov_b32_e32 v2, s26
	v_mov_b32_e32 v3, s23
	v_cmp_eq_u32_e64 s[64:65], 0, v233
	v_cmp_eq_u32_e64 s[66:67], 1, v233
	v_cmp_eq_u32_e64 s[68:69], 2, v233
	v_cmp_eq_u32_e64 s[70:71], 3, v233
	v_cndmask_b32_e64 v248, v2, v3, s[64:65]
	v_cndmask_b32_e64 v249, v2, v3, s[66:67]
	v_cndmask_b32_e64 v250, v2, v3, s[68:69]
	v_cndmask_b32_e64 v251, v2, v3, s[70:71]
	v_mul_f32_e32 v248, v1, v248
	v_mul_f32_e32 v249, v1, v249
	v_mul_f32_e32 v250, v1, v250
	v_mul_f32_e32 v251, v1, v251
	v_cndmask_b32_e64 v248, v0, v248, s[2:3]
	v_cndmask_b32_e64 v249, v0, v249, s[2:3]
	v_cndmask_b32_e64 v250, v0, v250, s[2:3]
	v_cndmask_b32_e64 v251, v0, v251, s[2:3]
	v_mul_f32_e32 v248, v248, v208
	v_mul_f32_e32 v249, v249, v209
	v_mul_f32_e32 v250, v250, v204
	v_mul_f32_e32 v251, v251, v205
	ds_write_b128 v238, v[248:251]
	v_cmp_eq_u32_e64 s[64:65], 4, v233
	v_cmp_eq_u32_e64 s[66:67], 5, v233
	v_cmp_eq_u32_e64 s[68:69], 6, v233
	v_cmp_eq_u32_e64 s[70:71], 7, v233
	v_cndmask_b32_e64 v248, v2, v3, s[64:65]
	v_cndmask_b32_e64 v249, v2, v3, s[66:67]
	v_cndmask_b32_e64 v250, v2, v3, s[68:69]
	v_cndmask_b32_e64 v251, v2, v3, s[70:71]
	v_mul_f32_e32 v248, v1, v248
	v_mul_f32_e32 v249, v1, v249
	v_mul_f32_e32 v250, v1, v250
	v_mul_f32_e32 v251, v1, v251
	v_cndmask_b32_e64 v248, v0, v248, s[2:3]
	v_cndmask_b32_e64 v249, v0, v249, s[2:3]
	v_cndmask_b32_e64 v250, v0, v250, s[2:3]
	v_cndmask_b32_e64 v251, v0, v251, s[2:3]
	v_mul_f32_e32 v248, v248, v182
	v_mul_f32_e32 v249, v249, v183
	v_mul_f32_e32 v250, v250, v178
	v_mul_f32_e32 v251, v251, v179
	ds_write_b128 v238, v[248:251] offset:32
	v_cmp_eq_u32_e64 s[64:65], 8, v233
	v_cmp_eq_u32_e64 s[66:67], 9, v233
	v_cmp_eq_u32_e64 s[68:69], 10, v233
	v_cmp_eq_u32_e64 s[70:71], 11, v233
	v_cndmask_b32_e64 v248, v2, v3, s[64:65]
	v_cndmask_b32_e64 v249, v2, v3, s[66:67]
	v_cndmask_b32_e64 v250, v2, v3, s[68:69]
	v_cndmask_b32_e64 v251, v2, v3, s[70:71]
	v_mul_f32_e32 v248, v1, v248
	v_mul_f32_e32 v249, v1, v249
	v_mul_f32_e32 v250, v1, v250
	v_mul_f32_e32 v251, v1, v251
	v_cndmask_b32_e64 v248, v0, v248, s[2:3]
	v_cndmask_b32_e64 v249, v0, v249, s[2:3]
	v_cndmask_b32_e64 v250, v0, v250, s[2:3]
	v_cndmask_b32_e64 v251, v0, v251, s[2:3]
	v_mul_f32_e32 v248, v248, v166
	v_mul_f32_e32 v249, v249, v167
	v_mul_f32_e32 v250, v250, v118
	v_mul_f32_e32 v251, v251, v119
	ds_write_b128 v238, v[248:251] offset:64
	v_cmp_eq_u32_e64 s[64:65], 12, v233
	v_cmp_eq_u32_e64 s[66:67], 13, v233
	v_cmp_eq_u32_e64 s[68:69], 14, v233
	v_cmp_eq_u32_e64 s[70:71], 15, v233
	v_cndmask_b32_e64 v248, v2, v3, s[64:65]
	v_cndmask_b32_e64 v249, v2, v3, s[66:67]
	v_cndmask_b32_e64 v250, v2, v3, s[68:69]
	v_cndmask_b32_e64 v251, v2, v3, s[70:71]
	v_mul_f32_e32 v248, v1, v248
	v_mul_f32_e32 v249, v1, v249
	v_mul_f32_e32 v250, v1, v250
	v_mul_f32_e32 v251, v1, v251
	v_cndmask_b32_e64 v248, v0, v248, s[2:3]
	v_cndmask_b32_e64 v249, v0, v249, s[2:3]
	v_cndmask_b32_e64 v250, v0, v250, s[2:3]
	v_cndmask_b32_e64 v251, v0, v251, s[2:3]
	v_mul_f32_e32 v248, v248, v116
	v_mul_f32_e32 v249, v249, v117
	v_mul_f32_e32 v250, v250, v114
	v_mul_f32_e32 v251, v251, v115
	ds_write_b128 v238, v[248:251] offset:96
	v_pk_mul_f32 v[248:249], v[0:1], v[112:113] op_sel_hi:[0,1]
	v_pk_mul_f32 v[250:251], v[0:1], v[98:99] op_sel_hi:[0,1]
	ds_write_b128 v238, v[248:251] offset:128
	v_pk_mul_f32 v[248:249], v[0:1], v[100:101] op_sel_hi:[0,1]
	v_pk_mul_f32 v[250:251], v[0:1], v[120:121] op_sel_hi:[0,1]
	ds_write_b128 v238, v[248:251] offset:160
	v_pk_mul_f32 v[248:249], v[0:1], v[102:103] op_sel_hi:[0,1]
	v_pk_mul_f32 v[250:251], v[0:1], v[122:123] op_sel_hi:[0,1]
	ds_write_b128 v238, v[248:251] offset:192
	v_pk_mul_f32 v[248:249], v[0:1], v[124:125] op_sel_hi:[0,1]
	v_pk_mul_f32 v[250:251], v[0:1], v[180:181] op_sel_hi:[0,1]
	ds_write_b128 v238, v[248:251] offset:224
	s_lshl_b32 s56, s56, 11
	s_add_i32 s56, s56, s25
	v_or_b32_e32 v252, s56, v239
	v_add_lshl_u32 v253, v241, s55, 7
	v_lshl_or_b32 v1, v252, 13, v240
	v_and_or_b32 v2, v253, s54, v1
	ds_read_b128 v[248:251], v246
	ds_read_b128 v[160:163], v246 offset:1088
	s_waitcnt lgkmcnt(1)
	global_store_dwordx4 v2, v[248:251], s[10:11] nt
	s_nop 0
	ds_read_b128 v[248:251], v246 offset:2176
	v_or_b32_e32 v3, 0x8000, v2
	s_waitcnt lgkmcnt(1)
	global_store_dwordx4 v3, v[160:163], s[10:11] nt
	s_nop 0
	ds_read_b128 v[160:163], v246 offset:3264
	v_or_b32_e32 v252, 0x10000, v2
	s_waitcnt lgkmcnt(1)
	global_store_dwordx4 v252, v[248:251], s[10:11] nt
	s_nop 0
	ds_read_b128 v[248:251], v246 offset:4352
	v_or_b32_e32 v3, 0x18000, v2
	s_waitcnt lgkmcnt(1)
	global_store_dwordx4 v3, v[160:163], s[10:11] nt
	s_nop 0
	ds_read_b128 v[160:163], v246 offset:5440
	v_or_b32_e32 v252, 0x20000, v2
	s_waitcnt lgkmcnt(1)
	global_store_dwordx4 v252, v[248:251], s[10:11] nt
	s_nop 0
	ds_read_b128 v[248:251], v246 offset:6528
	v_or_b32_e32 v3, 0x28000, v2
	s_waitcnt lgkmcnt(1)
	global_store_dwordx4 v3, v[160:163], s[10:11] nt
	s_nop 0
	ds_read_b128 v[160:163], v246 offset:7616
	v_or_b32_e32 v252, 0x30000, v2
	s_waitcnt lgkmcnt(1)
	global_store_dwordx4 v252, v[248:251], s[10:11] nt
	v_or_b32_e32 v3, 0x38000, v2
	s_waitcnt lgkmcnt(0)
	global_store_dwordx4 v3, v[160:163], s[10:11] nt
	v_pk_mul_f32 v[248:249], v[0:1], v[80:81] op_sel_hi:[0,1]
	v_pk_mul_f32 v[250:251], v[0:1], v[82:83] op_sel_hi:[0,1]
	ds_write_b128 v238, v[248:251]
	v_pk_mul_f32 v[248:249], v[0:1], v[84:85] op_sel_hi:[0,1]
	v_pk_mul_f32 v[250:251], v[0:1], v[96:97] op_sel_hi:[0,1]
	ds_write_b128 v238, v[248:251] offset:32
	v_pk_mul_f32 v[248:249], v[0:1], v[86:87] op_sel_hi:[0,1]
	v_pk_mul_f32 v[250:251], v[0:1], v[88:89] op_sel_hi:[0,1]
	ds_write_b128 v238, v[248:251] offset:64
	v_pk_mul_f32 v[248:249], v[0:1], v[90:91] op_sel_hi:[0,1]
	v_pk_mul_f32 v[250:251], v[0:1], v[94:95] op_sel_hi:[0,1]
	ds_write_b128 v238, v[248:251] offset:96
	v_pk_mul_f32 v[248:249], v[0:1], v[92:93] op_sel_hi:[0,1]
	v_pk_mul_f32 v[250:251], v[0:1], v[108:109] op_sel_hi:[0,1]
	ds_write_b128 v238, v[248:251] offset:128
	v_pk_mul_f32 v[248:249], v[0:1], v[110:111] op_sel_hi:[0,1]
	v_pk_mul_f32 v[250:251], v[0:1], v[176:177] op_sel_hi:[0,1]
	ds_write_b128 v238, v[248:251] offset:160
	v_pk_mul_f32 v[248:249], v[0:1], v[174:175] op_sel_hi:[0,1]
	v_pk_mul_f32 v[250:251], v[0:1], v[192:193] op_sel_hi:[0,1]
	ds_write_b128 v238, v[248:251] offset:192
	v_pk_mul_f32 v[248:249], v[0:1], v[194:195] op_sel_hi:[0,1]
	v_pk_mul_f32 v[250:251], v[0:1], v[206:207] op_sel_hi:[0,1]
	ds_write_b128 v238, v[248:251] offset:224
	v_add_u32_e32 v252, 0x100, v253
	v_and_or_b32 v2, v252, s54, v1
	ds_read_b128 v[248:251], v246
	ds_read_b128 v[160:163], v246 offset:1088
	s_waitcnt lgkmcnt(1)
	global_store_dwordx4 v2, v[248:251], s[10:11] nt
	s_nop 0
	ds_read_b128 v[248:251], v246 offset:2176
	v_or_b32_e32 v3, 0x8000, v2
	s_waitcnt lgkmcnt(1)
	global_store_dwordx4 v3, v[160:163], s[10:11] nt
	s_nop 0
	ds_read_b128 v[160:163], v246 offset:3264
	v_or_b32_e32 v252, 0x10000, v2
	s_waitcnt lgkmcnt(1)
	global_store_dwordx4 v252, v[248:251], s[10:11] nt
	s_nop 0
	ds_read_b128 v[248:251], v246 offset:4352
	v_or_b32_e32 v3, 0x18000, v2
	s_waitcnt lgkmcnt(1)
	global_store_dwordx4 v3, v[160:163], s[10:11] nt
	s_nop 0
	ds_read_b128 v[160:163], v246 offset:5440
	v_or_b32_e32 v252, 0x20000, v2
	s_waitcnt lgkmcnt(1)
	global_store_dwordx4 v252, v[248:251], s[10:11] nt
	s_nop 0
	ds_read_b128 v[248:251], v246 offset:6528
	v_or_b32_e32 v3, 0x28000, v2
	s_waitcnt lgkmcnt(1)
	global_store_dwordx4 v3, v[160:163], s[10:11] nt
	s_nop 0
	ds_read_b128 v[160:163], v246 offset:7616
	v_or_b32_e32 v252, 0x30000, v2
	s_waitcnt lgkmcnt(1)
	global_store_dwordx4 v252, v[248:251], s[10:11] nt
	v_or_b32_e32 v3, 0x38000, v2
	s_waitcnt lgkmcnt(0)
	global_store_dwordx4 v3, v[160:163], s[10:11] nt
	s_add_i32 s63, s62, 0x3000
	s_and_b32 s63, s63, 0x3f000
	s_or_b32 s63, s63, s58
	v_or_b32_e32 v2, s63, v231
	global_load_dwordx4 v[80:83], v2, s[6:7]
	global_load_dwordx4 v[84:87], v2, s[6:7] offset:1024
	global_load_dwordx4 v[88:91], v2, s[6:7] offset:2048
	global_load_dwordx4 v[92:95], v2, s[6:7] offset:3072
	s_add_i32 s63, s62, 0x2000
	s_and_b32 s63, s63, 0x3f000
	s_or_b32 s63, s63, s58
	v_or_b32_e32 v3, s63, v231
	global_load_dwordx4 v[96:99], v3, s[6:7]
	global_load_dwordx4 v[100:103], v3, s[6:7] offset:1024
	global_load_dwordx4 v[108:111], v3, s[6:7] offset:2048
	global_load_dwordx4 v[192:195], v3, s[6:7] offset:3072
	s_add_i32 s63, s62, 0x1000
	s_and_b32 s63, s63, 0x3f000
	s_or_b32 s63, s63, s58
	v_or_b32_e32 v2, s63, v231
	global_load_dwordx4 v[174:177], v2, s[6:7] offset:2048
	global_load_dwordx4 v[178:181], v2, s[6:7] offset:3072
	v_pk_mul_f32 v[248:249], v[0:1], v[64:65] op_sel_hi:[0,1]
	v_pk_mul_f32 v[250:251], v[0:1], v[66:67] op_sel_hi:[0,1]
	ds_write_b128 v238, v[248:251]
	v_pk_mul_f32 v[248:249], v[0:1], v[68:69] op_sel_hi:[0,1]
	v_pk_mul_f32 v[250:251], v[0:1], v[74:75] op_sel_hi:[0,1]
	ds_write_b128 v238, v[248:251] offset:32
	v_pk_mul_f32 v[248:249], v[0:1], v[72:73] op_sel_hi:[0,1]
	v_pk_mul_f32 v[250:251], v[0:1], v[104:105] op_sel_hi:[0,1]
	ds_write_b128 v238, v[248:251] offset:64
	v_pk_mul_f32 v[248:249], v[0:1], v[106:107] op_sel_hi:[0,1]
	v_pk_mul_f32 v[250:251], v[0:1], v[172:173] op_sel_hi:[0,1]
	ds_write_b128 v238, v[248:251] offset:96
	v_pk_mul_f32 v[248:249], v[0:1], v[170:171] op_sel_hi:[0,1]
	v_pk_mul_f32 v[250:251], v[0:1], v[188:189] op_sel_hi:[0,1]
	ds_write_b128 v238, v[248:251] offset:128
	v_pk_mul_f32 v[248:249], v[0:1], v[190:191] op_sel_hi:[0,1]
	v_pk_mul_f32 v[250:251], v[0:1], v[202:203] op_sel_hi:[0,1]
	ds_write_b128 v238, v[248:251] offset:160
	v_pk_mul_f32 v[248:249], v[0:1], v[200:201] op_sel_hi:[0,1]
	v_pk_mul_f32 v[250:251], v[0:1], v[214:215] op_sel_hi:[0,1]
	ds_write_b128 v238, v[248:251] offset:192
	v_pk_mul_f32 v[248:249], v[0:1], v[216:217] op_sel_hi:[0,1]
	v_pk_mul_f32 v[250:251], v[0:1], v[222:223] op_sel_hi:[0,1]
	ds_write_b128 v238, v[248:251] offset:224
	v_add_u32_e32 v252, 0x200, v253
	v_and_or_b32 v2, v252, s54, v1
	ds_read_b128 v[248:251], v246
	ds_read_b128 v[160:163], v246 offset:1088
	s_waitcnt lgkmcnt(1)
	global_store_dwordx4 v2, v[248:251], s[10:11] nt
	s_nop 0
	ds_read_b128 v[248:251], v246 offset:2176
	v_or_b32_e32 v3, 0x8000, v2
	s_waitcnt lgkmcnt(1)
	global_store_dwordx4 v3, v[160:163], s[10:11] nt
	s_nop 0
	ds_read_b128 v[160:163], v246 offset:3264
	v_or_b32_e32 v252, 0x10000, v2
	s_waitcnt lgkmcnt(1)
	global_store_dwordx4 v252, v[248:251], s[10:11] nt
	s_nop 0
	ds_read_b128 v[248:251], v246 offset:4352
	v_or_b32_e32 v3, 0x18000, v2
	s_waitcnt lgkmcnt(1)
	global_store_dwordx4 v3, v[160:163], s[10:11] nt
	s_nop 0
	ds_read_b128 v[160:163], v246 offset:5440
	v_or_b32_e32 v252, 0x20000, v2
	s_waitcnt lgkmcnt(1)
	global_store_dwordx4 v252, v[248:251], s[10:11] nt
	s_nop 0
	ds_read_b128 v[248:251], v246 offset:6528
	v_or_b32_e32 v3, 0x28000, v2
	s_waitcnt lgkmcnt(1)
	global_store_dwordx4 v3, v[160:163], s[10:11] nt
	s_nop 0
	ds_read_b128 v[160:163], v246 offset:7616
	v_or_b32_e32 v252, 0x30000, v2
	s_waitcnt lgkmcnt(1)
	global_store_dwordx4 v252, v[248:251], s[10:11] nt
	v_or_b32_e32 v3, 0x38000, v2
	s_waitcnt lgkmcnt(0)
	global_store_dwordx4 v3, v[160:163], s[10:11] nt
	v_pk_mul_f32 v[248:249], v[0:1], v[70:71] op_sel_hi:[0,1]
	v_pk_mul_f32 v[250:251], v[0:1], v[76:77] op_sel_hi:[0,1]
	ds_write_b128 v238, v[248:251]
	v_pk_mul_f32 v[248:249], v[0:1], v[78:79] op_sel_hi:[0,1]
	v_pk_mul_f32 v[250:251], v[0:1], v[168:169] op_sel_hi:[0,1]
	ds_write_b128 v238, v[248:251] offset:32
	v_pk_mul_f32 v[248:249], v[0:1], v[126:127] op_sel_hi:[0,1]
	v_pk_mul_f32 v[250:251], v[0:1], v[184:185] op_sel_hi:[0,1]
	ds_write_b128 v238, v[248:251] offset:64
	v_pk_mul_f32 v[248:249], v[0:1], v[186:187] op_sel_hi:[0,1]
	v_pk_mul_f32 v[250:251], v[0:1], v[198:199] op_sel_hi:[0,1]
	ds_write_b128 v238, v[248:251] offset:96
	v_pk_mul_f32 v[248:249], v[0:1], v[196:197] op_sel_hi:[0,1]
	v_pk_mul_f32 v[250:251], v[0:1], v[210:211] op_sel_hi:[0,1]
	ds_write_b128 v238, v[248:251] offset:128
	v_pk_mul_f32 v[248:249], v[0:1], v[212:213] op_sel_hi:[0,1]
	v_pk_mul_f32 v[250:251], v[0:1], v[220:221] op_sel_hi:[0,1]
	ds_write_b128 v238, v[248:251] offset:160
	v_pk_mul_f32 v[248:249], v[0:1], v[218:219] op_sel_hi:[0,1]
	v_pk_mul_f32 v[250:251], v[0:1], v[224:225] op_sel_hi:[0,1]
	ds_write_b128 v238, v[248:251] offset:192
	v_pk_mul_f32 v[248:249], v[0:1], v[226:227] op_sel_hi:[0,1]
	v_pk_mul_f32 v[250:251], v[0:1], v[228:229] op_sel_hi:[0,1]
	ds_write_b128 v238, v[248:251] offset:224
	v_add_u32_e32 v252, 0x300, v253
	v_and_or_b32 v2, v252, s54, v1
	ds_read_b128 v[248:251], v246
	ds_read_b128 v[160:163], v246 offset:1088
	s_waitcnt lgkmcnt(1)
	global_store_dwordx4 v2, v[248:251], s[10:11] nt
	s_nop 0
	ds_read_b128 v[248:251], v246 offset:2176
	v_or_b32_e32 v3, 0x8000, v2
	s_waitcnt lgkmcnt(1)
	global_store_dwordx4 v3, v[160:163], s[10:11] nt
	s_nop 0
	ds_read_b128 v[160:163], v246 offset:3264
	v_or_b32_e32 v252, 0x10000, v2
	s_waitcnt lgkmcnt(1)
	global_store_dwordx4 v252, v[248:251], s[10:11] nt
	s_nop 0
	ds_read_b128 v[248:251], v246 offset:4352
	v_or_b32_e32 v3, 0x18000, v2
	s_waitcnt lgkmcnt(1)
	global_store_dwordx4 v3, v[160:163], s[10:11] nt
	s_nop 0
	ds_read_b128 v[160:163], v246 offset:5440
	v_or_b32_e32 v252, 0x20000, v2
	s_waitcnt lgkmcnt(1)
	global_store_dwordx4 v252, v[248:251], s[10:11] nt
	s_nop 0
	ds_read_b128 v[248:251], v246 offset:6528
	v_or_b32_e32 v3, 0x28000, v2
	s_waitcnt lgkmcnt(1)
	global_store_dwordx4 v3, v[160:163], s[10:11] nt
	s_nop 0
	ds_read_b128 v[160:163], v246 offset:7616
	v_or_b32_e32 v252, 0x30000, v2
	s_waitcnt lgkmcnt(1)
	global_store_dwordx4 v252, v[248:251], s[10:11] nt
	v_or_b32_e32 v3, 0x38000, v2
	s_waitcnt lgkmcnt(0)
	global_store_dwordx4 v3, v[160:163], s[10:11] nt
	s_mov_b32 s57, s24
	s_add_i32 s12, s12, 4
	s_cmp_eq_u32 s12, 32
	s_cbranch_scc1 .LBB1_22
.LBB1_14:
	s_and_b32 s24, s12, 24
	s_or_b32 s56, s24, s27
	s_and_b32 s24, s57, 1
	s_or_b32 s55, s24, s28
	s_add_i32 s24, s55, s29
	s_lshl_b32 s24, s24, 12
	s_lshl_b32 s58, s56, 18
	ds_read_b128 v[64:67], v243
	ds_read_b128 v[68:71], v243 offset:16
	s_waitcnt lgkmcnt(1)
	v_pk_mul_f32 v[76:77], v[64:65], s[22:23] op_sel_hi:[1,0]
	s_waitcnt lgkmcnt(0)
	v_pk_mul_f32 v[64:65], v[68:69], s[22:23] op_sel_hi:[1,0]
	v_pk_mul_f32 v[78:79], v[66:67], s[22:23] op_sel_hi:[1,0]
	v_pk_mul_f32 v[74:75], v[70:71], s[22:23] op_sel_hi:[1,0]
	v_cvt_pk_f16_f32 v204, v64, v65
	ds_read_b128 v[64:67], v243 offset:64
	ds_read_b128 v[68:71], v243 offset:80
	v_cvt_pk_f16_f32 v202, v76, v77
	v_cvt_pk_f16_f32 v205, v74, v75
	v_cvt_pk_f16_f32 v203, v78, v79
	s_waitcnt lgkmcnt(1)
	v_pk_mul_f32 v[76:77], v[64:65], s[22:23] op_sel_hi:[1,0]
	s_waitcnt lgkmcnt(0)
	v_pk_mul_f32 v[64:65], v[68:69], s[22:23] op_sel_hi:[1,0]
	v_pk_mul_f32 v[78:79], v[66:67], s[22:23] op_sel_hi:[1,0]
	v_pk_mul_f32 v[74:75], v[70:71], s[22:23] op_sel_hi:[1,0]
	v_cvt_pk_f16_f32 v208, v64, v65
	ds_read_b128 v[64:67], v243 offset:128
	ds_read_b128 v[68:71], v243 offset:144
	v_cvt_pk_f16_f32 v206, v76, v77
	v_cvt_pk_f16_f32 v209, v74, v75
	v_cvt_pk_f16_f32 v207, v78, v79
	s_waitcnt lgkmcnt(1)
	v_pk_mul_f32 v[76:77], v[64:65], s[22:23] op_sel_hi:[1,0]
	s_waitcnt lgkmcnt(0)
	v_pk_mul_f32 v[64:65], v[68:69], s[22:23] op_sel_hi:[1,0]
	v_pk_mul_f32 v[78:79], v[66:67], s[22:23] op_sel_hi:[1,0]
	v_pk_mul_f32 v[74:75], v[70:71], s[22:23] op_sel_hi:[1,0]
	v_cvt_pk_f16_f32 v212, v64, v65
	ds_read_b128 v[64:67], v243 offset:192
	ds_read_b128 v[68:71], v243 offset:208
	v_cvt_pk_f16_f32 v211, v78, v79
	v_cvt_pk_f16_f32 v210, v76, v77
	v_cvt_pk_f16_f32 v213, v74, v75
	s_waitcnt lgkmcnt(1)
	v_pk_mul_f32 v[78:79], v[66:67], s[22:23] op_sel_hi:[1,0]
	s_waitcnt lgkmcnt(0)
	v_pk_mul_f32 v[66:67], v[70:71], s[22:23] op_sel_hi:[1,0]
	v_pk_mul_f32 v[64:65], v[64:65], s[22:23] op_sel_hi:[1,0]
	v_pk_mul_f32 v[68:69], v[68:69], s[22:23] op_sel_hi:[1,0]
	v_cvt_pk_f16_f32 v214, v64, v65
	v_cvt_pk_f16_f32 v216, v68, v69
	v_cvt_pk_f16_f32 v217, v66, v67
	v_cvt_pk_f16_f32 v215, v78, v79
	s_waitcnt vmcnt(57)
	v_mfma_f32_32x32x16_f16 v[112:127], v[48:51], v[202:205], 0
	v_mfma_f32_32x32x16_f16 v[112:127], v[52:55], v[206:209], v[112:127]
	v_mfma_f32_32x32x16_f16 v[112:127], v[56:59], v[210:213], v[112:127]
	v_mfma_f32_32x32x16_f16 v[112:127], v[60:63], v[214:217], v[112:127]
	s_waitcnt vmcnt(50)
	v_mfma_f32_32x32x16_f16 v[48:63], v[32:35], v[202:205], 0
	s_waitcnt vmcnt(49)
	v_mfma_f32_32x32x16_f16 v[48:63], v[36:39], v[206:209], v[48:63]
	v_mfma_f32_32x32x16_f16 v[48:63], v[40:43], v[210:213], v[48:63]
	v_mfma_f32_32x32x16_f16 v[48:63], v[44:47], v[214:217], v[48:63]
	s_waitcnt vmcnt(48)
	v_mfma_f32_32x32x16_f16 v[32:47], v[16:19], v[202:205], 0
	s_waitcnt vmcnt(47)
	v_mfma_f32_32x32x16_f16 v[32:47], v[20:23], v[206:209], v[32:47]
	s_waitcnt vmcnt(46)
	v_mfma_f32_32x32x16_f16 v[32:47], v[24:27], v[210:213], v[32:47]
	s_waitcnt vmcnt(45)
	v_mfma_f32_32x32x16_f16 v[32:47], v[28:31], v[214:217], v[32:47]
	s_waitcnt vmcnt(44)
	v_mfma_f32_32x32x16_f16 v[16:31], v[4:7], v[202:205], 0
	s_waitcnt vmcnt(43)
	v_mfma_f32_32x32x16_f16 v[16:31], v[8:11], v[206:209], v[16:31]
	s_waitcnt vmcnt(42)
	v_mfma_f32_32x32x16_f16 v[16:31], v[12:15], v[210:213], v[16:31]
	v_mfma_f32_32x32x16_f16 v[16:31], v[148:151], v[214:217], v[16:31]
	v_mfma_f32_32x32x16_f16 v[0:15], v[132:135], v[202:205], 0
	v_mfma_f32_32x32x16_f16 v[0:15], v[136:139], v[206:209], v[0:15]
	v_mfma_f32_32x32x16_f16 v[0:15], v[140:143], v[210:213], v[0:15]
	v_mfma_f32_32x32x16_f16 v[0:15], v[144:147], v[214:217], v[0:15]
	s_waitcnt vmcnt(25)
	v_mfma_f32_32x32x16_f16 v[64:79], v[80:83], v[202:205], 0
	s_waitcnt vmcnt(24)
	v_mfma_f32_32x32x16_f16 v[64:79], v[84:87], v[206:209], v[64:79]
	s_waitcnt vmcnt(23)
	v_mfma_f32_32x32x16_f16 v[64:79], v[88:91], v[210:213], v[64:79]
	s_waitcnt vmcnt(22)
	v_mfma_f32_32x32x16_f16 v[64:79], v[92:95], v[214:217], v[64:79]
	s_waitcnt vmcnt(21)
	v_mfma_f32_32x32x16_f16 v[80:95], v[96:99], v[202:205], 0
	s_waitcnt vmcnt(20)
	v_mfma_f32_32x32x16_f16 v[80:95], v[100:103], v[206:209], v[80:95]
	s_waitcnt vmcnt(19)
	v_mfma_f32_32x32x16_f16 v[80:95], v[108:111], v[210:213], v[80:95]
	s_waitcnt vmcnt(18)
	v_mfma_f32_32x32x16_f16 v[80:95], v[192:195], v[214:217], v[80:95]
	v_mfma_f32_32x32x16_f16 v[96:111], v[152:155], v[202:205], 0
	v_mfma_f32_32x32x16_f16 v[96:111], v[156:159], v[206:209], v[96:111]
	s_waitcnt vmcnt(17)
	v_mfma_f32_32x32x16_f16 v[96:111], v[174:177], v[210:213], v[96:111]
	s_waitcnt vmcnt(16)
	v_mfma_f32_32x32x16_f16 v[96:111], v[178:181], v[214:217], v[96:111]
	s_and_b32 s25, s24, 0x3f000
	s_addk_i32 s24, 0x1000
	s_or_b32 s25, s58, s25
	s_and_b32 s24, s24, 0x3f000
	v_or_b32_e32 v132, s25, v231
	s_or_b32 s24, s58, s24
	global_load_dwordx4 v[156:159], v132, s[16:17]
	global_load_dwordx4 v[160:163], v132, s[16:17] offset:1024
	global_load_dwordx4 v[152:155], v132, s[16:17] offset:2048
	global_load_dwordx4 v[148:151], v132, s[16:17] offset:3072
	v_or_b32_e32 v132, s24, v231
	global_load_dwordx4 v[144:147], v132, s[16:17]
	global_load_dwordx4 v[140:143], v132, s[16:17] offset:1024
	global_load_dwordx4 v[136:139], v132, s[16:17] offset:2048
	s_nop 0
	global_load_dwordx4 v[132:135], v132, s[16:17] offset:3072
	v_max_f32_e32 v166, v113, v113
	v_max_f32_e32 v167, v112, v112
	v_max_f32_e32 v166, v167, v166
	v_max3_f32 v166, v166, v114, v115
	v_max3_f32 v166, v166, v116, v117
	v_max3_f32 v166, v166, v118, v119
	v_max3_f32 v166, v166, v120, v121
	v_max3_f32 v166, v166, v122, v123
	v_max3_f32 v166, v166, v124, v125
	v_max3_f32 v166, v166, v126, v127
	v_max3_f32 v166, v166, v96, v97
	v_max3_f32 v166, v166, v98, v99
	v_max3_f32 v166, v166, v100, v101
	v_max3_f32 v166, v166, v102, v103
	v_max3_f32 v166, v166, v104, v105
	v_max3_f32 v166, v166, v106, v107
	v_max3_f32 v166, v166, v108, v109
	v_max3_f32 v166, v166, v110, v111
	v_max3_f32 v166, v166, v80, v81
	v_max3_f32 v166, v166, v82, v83
	v_max3_f32 v166, v166, v84, v85
	v_max3_f32 v166, v166, v86, v87
	v_max3_f32 v166, v166, v88, v89
	v_max3_f32 v166, v166, v90, v91
	v_max3_f32 v166, v166, v92, v93
	v_max3_f32 v166, v166, v94, v95
	v_max3_f32 v166, v166, v64, v65
	v_max3_f32 v166, v166, v66, v67
	v_max3_f32 v166, v166, v68, v69
	v_max3_f32 v166, v166, v70, v71
	v_max3_f32 v166, v166, v72, v73
	v_max3_f32 v166, v166, v74, v75
	v_max3_f32 v166, v166, v76, v77
	v_max3_f32 v166, v166, v78, v79
	v_max3_f32 v166, v166, v48, v49
	v_max3_f32 v166, v166, v50, v51
	v_max3_f32 v166, v166, v52, v53
	v_max3_f32 v166, v166, v54, v55
	v_max3_f32 v166, v166, v56, v57
	v_max3_f32 v166, v166, v58, v59
	v_max3_f32 v166, v166, v60, v61
	v_max3_f32 v166, v166, v62, v63
	v_max3_f32 v166, v166, v32, v33
	v_max3_f32 v166, v166, v34, v35
	v_max3_f32 v166, v166, v36, v37
	v_max3_f32 v166, v166, v38, v39
	v_max3_f32 v166, v166, v40, v41
	v_max3_f32 v166, v166, v42, v43
	v_max3_f32 v166, v166, v44, v45
	v_max3_f32 v166, v166, v46, v47
	v_max3_f32 v166, v166, v16, v17
	v_max3_f32 v166, v166, v18, v19
	v_max3_f32 v166, v166, v20, v21
	v_max3_f32 v166, v166, v22, v23
	v_max3_f32 v166, v166, v24, v25
	v_max3_f32 v166, v166, v26, v27
	v_max3_f32 v166, v166, v28, v29
	v_max3_f32 v166, v166, v30, v31
	v_max3_f32 v166, v166, v0, v1
	v_max3_f32 v166, v166, v2, v3
	v_max3_f32 v166, v166, v4, v5
	v_max3_f32 v166, v166, v6, v7
	v_max3_f32 v166, v166, v8, v9
	v_max3_f32 v166, v166, v10, v11
	v_max3_f32 v166, v166, v12, v13
	v_max3_f32 v166, v166, v14, v15
	ds_bpermute_b32 v167, v234, v166
	s_waitcnt lgkmcnt(0)
	v_max_f32_e32 v167, v167, v167
	v_max_f32_e32 v247, v166, v167
	s_and_saveexec_b64 s[24:25], s[0:1]
	v_add_u32_e32 v166, s31, v235
	ds_write_b32 v166, v247
	s_or_b64 exec, exec, s[24:25]
	v_sub_f32_e32 v112, v112, v247
	v_exp_f32_e32 v208, v112
	v_sub_f32_e32 v112, v113, v247
	v_exp_f32_e32 v209, v112
	v_sub_f32_e32 v112, v114, v247
	v_exp_f32_e32 v204, v112
	v_sub_f32_e32 v112, v115, v247
	v_exp_f32_e32 v205, v112
	v_sub_f32_e32 v113, v116, v247
	v_add_f32_e32 v112, 0, v208
	v_exp_f32_e32 v182, v113
	v_sub_f32_e32 v113, v117, v247
	v_add_f32_e32 v112, v112, v209
	v_exp_f32_e32 v183, v113
	v_sub_f32_e32 v113, v118, v247
	v_add_f32_e32 v112, v112, v204
	v_exp_f32_e32 v178, v113
	v_sub_f32_e32 v113, v119, v247
	v_add_f32_e32 v112, v112, v205
	v_exp_f32_e32 v179, v113
	v_sub_f32_e32 v113, v120, v247
	v_add_f32_e32 v112, v112, v182
	v_exp_f32_e32 v166, v113
	v_sub_f32_e32 v113, v121, v247
	v_add_f32_e32 v112, v112, v183
	v_exp_f32_e32 v167, v113
	v_sub_f32_e32 v113, v122, v247
	v_add_f32_e32 v112, v112, v178
	v_exp_f32_e32 v118, v113
	v_sub_f32_e32 v113, v123, v247
	v_add_f32_e32 v112, v112, v179
	v_exp_f32_e32 v119, v113
	v_sub_f32_e32 v113, v124, v247
	v_add_f32_e32 v112, v112, v166
	v_exp_f32_e32 v116, v113
	v_sub_f32_e32 v113, v125, v247
	v_add_f32_e32 v112, v112, v167
	v_exp_f32_e32 v117, v113
	v_sub_f32_e32 v113, v126, v247
	v_add_f32_e32 v112, v112, v118
	v_exp_f32_e32 v114, v113
	v_sub_f32_e32 v113, v127, v247
	v_add_f32_e32 v112, v112, v119
	v_exp_f32_e32 v115, v113
	v_add_f32_e32 v112, v112, v116
	v_add_f32_e32 v112, v112, v117
	v_add_f32_e32 v112, v112, v114
	v_sub_f32_e32 v96, v96, v247
	v_add_f32_e32 v120, v112, v115
	v_exp_f32_e32 v112, v96
	v_sub_f32_e32 v96, v97, v247
	v_exp_f32_e32 v113, v96
	v_sub_f32_e32 v96, v98, v247
	v_exp_f32_e32 v98, v96
	v_sub_f32_e32 v96, v99, v247
	v_exp_f32_e32 v99, v96
	v_sub_f32_e32 v97, v100, v247
	v_add_f32_e32 v96, v120, v112
	v_exp_f32_e32 v100, v97
	v_sub_f32_e32 v97, v101, v247
	v_add_f32_e32 v96, v96, v113
	v_exp_f32_e32 v101, v97
	v_sub_f32_e32 v97, v102, v247
	v_add_f32_e32 v96, v96, v98
	v_exp_f32_e32 v120, v97
	v_sub_f32_e32 v97, v103, v247
	v_add_f32_e32 v96, v96, v99
	v_exp_f32_e32 v121, v97
	v_sub_f32_e32 v97, v104, v247
	v_add_f32_e32 v96, v96, v100
	v_exp_f32_e32 v102, v97
	v_sub_f32_e32 v97, v105, v247
	v_add_f32_e32 v96, v96, v101
	v_exp_f32_e32 v103, v97
	v_sub_f32_e32 v97, v106, v247
	v_add_f32_e32 v96, v96, v120
	v_exp_f32_e32 v122, v97
	v_sub_f32_e32 v97, v107, v247
	v_add_f32_e32 v96, v96, v121
	v_exp_f32_e32 v123, v97
	v_sub_f32_e32 v97, v108, v247
	v_add_f32_e32 v96, v96, v102
	v_exp_f32_e32 v124, v97
	v_sub_f32_e32 v97, v109, v247
	v_add_f32_e32 v96, v96, v103
	v_exp_f32_e32 v125, v97
	v_sub_f32_e32 v97, v110, v247
	v_add_f32_e32 v96, v96, v122
	v_exp_f32_e32 v180, v97
	v_sub_f32_e32 v97, v111, v247
	v_add_f32_e32 v96, v96, v123
	v_exp_f32_e32 v181, v97
	v_sub_f32_e32 v80, v80, v247
	v_add_f32_e32 v96, v96, v124
	v_exp_f32_e32 v80, v80
	v_sub_f32_e32 v81, v81, v247
	v_add_f32_e32 v96, v96, v125
	v_exp_f32_e32 v81, v81
	v_sub_f32_e32 v82, v82, v247
	v_add_f32_e32 v96, v96, v180
	v_exp_f32_e32 v82, v82
	v_sub_f32_e32 v83, v83, v247
	v_add_f32_e32 v96, v96, v181
	v_exp_f32_e32 v83, v83
	v_add_f32_e32 v96, v96, v80
	v_sub_f32_e32 v84, v84, v247
	v_add_f32_e32 v96, v96, v81
	v_exp_f32_e32 v84, v84
	v_sub_f32_e32 v85, v85, v247
	v_add_f32_e32 v96, v96, v82
	v_exp_f32_e32 v85, v85
	v_sub_f32_e32 v86, v86, v247
	v_add_f32_e32 v104, v96, v83
	v_exp_f32_e32 v96, v86
	v_sub_f32_e32 v86, v87, v247
	v_exp_f32_e32 v97, v86
	v_add_f32_e32 v86, v104, v84
	v_add_f32_e32 v86, v86, v85
	v_add_f32_e32 v86, v86, v96
	v_add_f32_e32 v104, v86, v97
	v_sub_f32_e32 v86, v88, v247
	v_exp_f32_e32 v86, v86
	v_sub_f32_e32 v87, v89, v247
	v_exp_f32_e32 v87, v87
	v_sub_f32_e32 v88, v90, v247
	v_exp_f32_e32 v88, v88
	v_sub_f32_e32 v89, v91, v247
	v_exp_f32_e32 v89, v89
	v_add_f32_e32 v90, v104, v86
	v_add_f32_e32 v90, v90, v87
	v_add_f32_e32 v90, v90, v88
	v_add_f32_e32 v104, v90, v89
	v_sub_f32_e32 v90, v92, v247
	v_exp_f32_e32 v90, v90
	v_sub_f32_e32 v91, v93, v247
	v_exp_f32_e32 v91, v91
	v_sub_f32_e32 v92, v94, v247
	v_exp_f32_e32 v94, v92
	v_sub_f32_e32 v92, v95, v247
	v_exp_f32_e32 v95, v92
	v_add_f32_e32 v92, v104, v90
	v_add_f32_e32 v92, v92, v91
	v_add_f32_e32 v92, v92, v94
	v_sub_f32_e32 v64, v64, v247
	v_add_f32_e32 v104, v92, v95
	v_exp_f32_e32 v92, v64
	v_sub_f32_e32 v64, v65, v247
	v_exp_f32_e32 v93, v64
	v_sub_f32_e32 v64, v66, v247
	v_exp_f32_e32 v108, v64
	v_sub_f32_e32 v64, v67, v247
	v_exp_f32_e32 v109, v64
	v_sub_f32_e32 v65, v68, v247
	v_add_f32_e32 v64, v104, v92
	v_exp_f32_e32 v110, v65
	v_sub_f32_e32 v65, v69, v247
	v_add_f32_e32 v64, v64, v93
	v_exp_f32_e32 v111, v65
	v_sub_f32_e32 v65, v70, v247
	v_add_f32_e32 v64, v64, v108
	v_exp_f32_e32 v176, v65
	v_sub_f32_e32 v65, v71, v247
	v_add_f32_e32 v64, v64, v109
	v_exp_f32_e32 v177, v65
	v_sub_f32_e32 v65, v72, v247
	v_add_f32_e32 v64, v64, v110
	v_exp_f32_e32 v174, v65
	v_sub_f32_e32 v65, v73, v247
	v_add_f32_e32 v64, v64, v111
	v_exp_f32_e32 v175, v65
	v_sub_f32_e32 v65, v74, v247
	v_add_f32_e32 v64, v64, v176
	v_exp_f32_e32 v192, v65
	v_sub_f32_e32 v65, v75, v247
	v_add_f32_e32 v64, v64, v177
	v_exp_f32_e32 v193, v65
	v_sub_f32_e32 v65, v76, v247
	v_add_f32_e32 v64, v64, v174
	v_exp_f32_e32 v194, v65
	v_sub_f32_e32 v65, v77, v247
	v_add_f32_e32 v64, v64, v175
	v_exp_f32_e32 v195, v65
	v_sub_f32_e32 v65, v78, v247
	v_add_f32_e32 v64, v64, v192
	v_exp_f32_e32 v206, v65
	v_sub_f32_e32 v65, v79, v247
	v_add_f32_e32 v64, v64, v193
	v_exp_f32_e32 v207, v65
	v_add_f32_e32 v64, v64, v194
	v_add_f32_e32 v64, v64, v195
	v_add_f32_e32 v64, v64, v206
	v_sub_f32_e32 v48, v48, v247
	v_add_f32_e32 v68, v64, v207
	v_exp_f32_e32 v64, v48
	v_sub_f32_e32 v48, v49, v247
	v_exp_f32_e32 v65, v48
	v_sub_f32_e32 v48, v50, v247
	v_exp_f32_e32 v66, v48
	v_sub_f32_e32 v48, v51, v247
	v_exp_f32_e32 v67, v48
	v_sub_f32_e32 v49, v52, v247
	v_add_f32_e32 v48, v68, v64
	v_exp_f32_e32 v68, v49
	v_sub_f32_e32 v49, v53, v247
	v_add_f32_e32 v48, v48, v65
	v_exp_f32_e32 v69, v49
	v_sub_f32_e32 v49, v54, v247
	v_add_f32_e32 v48, v48, v66
	v_exp_f32_e32 v74, v49
	v_sub_f32_e32 v49, v55, v247
	v_add_f32_e32 v48, v48, v67
	v_exp_f32_e32 v75, v49
	v_sub_f32_e32 v49, v56, v247
	v_add_f32_e32 v48, v48, v68
	v_exp_f32_e32 v72, v49
	v_sub_f32_e32 v49, v57, v247
	v_add_f32_e32 v48, v48, v69
	v_exp_f32_e32 v73, v49
	v_sub_f32_e32 v49, v58, v247
	v_add_f32_e32 v48, v48, v74
	v_exp_f32_e32 v104, v49
	v_sub_f32_e32 v49, v59, v247
	v_add_f32_e32 v48, v48, v75
	v_exp_f32_e32 v105, v49
	v_sub_f32_e32 v49, v60, v247
	v_add_f32_e32 v48, v48, v72
	v_exp_f32_e32 v106, v49
	v_sub_f32_e32 v49, v61, v247
	v_add_f32_e32 v48, v48, v73
	v_exp_f32_e32 v107, v49
	v_sub_f32_e32 v49, v62, v247
	v_add_f32_e32 v48, v48, v104
	v_exp_f32_e32 v172, v49
	v_sub_f32_e32 v49, v63, v247
	v_add_f32_e32 v48, v48, v105
	v_exp_f32_e32 v173, v49
	v_sub_f32_e32 v32, v32, v247
	v_add_f32_e32 v48, v48, v106
	v_exp_f32_e32 v170, v32
	v_sub_f32_e32 v32, v33, v247
	v_add_f32_e32 v48, v48, v107
	v_exp_f32_e32 v171, v32
	v_sub_f32_e32 v32, v34, v247
	v_add_f32_e32 v48, v48, v172
	v_exp_f32_e32 v188, v32
	v_sub_f32_e32 v32, v35, v247
	v_add_f32_e32 v48, v48, v173
	v_exp_f32_e32 v189, v32
	v_sub_f32_e32 v33, v36, v247
	v_add_f32_e32 v32, v48, v170
	v_exp_f32_e32 v190, v33
	v_sub_f32_e32 v33, v37, v247
	v_add_f32_e32 v32, v32, v171
	v_exp_f32_e32 v191, v33
	v_sub_f32_e32 v33, v38, v247
	v_add_f32_e32 v32, v32, v188
	v_exp_f32_e32 v202, v33
	v_sub_f32_e32 v33, v39, v247
	v_add_f32_e32 v32, v32, v189
	v_exp_f32_e32 v203, v33
	v_sub_f32_e32 v33, v40, v247
	v_add_f32_e32 v32, v32, v190
	v_exp_f32_e32 v200, v33
	v_sub_f32_e32 v33, v41, v247
	v_add_f32_e32 v32, v32, v191
	v_exp_f32_e32 v201, v33
	v_sub_f32_e32 v33, v42, v247
	v_add_f32_e32 v32, v32, v202
	v_exp_f32_e32 v214, v33
	v_sub_f32_e32 v33, v43, v247
	v_add_f32_e32 v32, v32, v203
	v_exp_f32_e32 v215, v33
	v_sub_f32_e32 v33, v44, v247
	v_add_f32_e32 v32, v32, v200
	v_exp_f32_e32 v216, v33
	v_sub_f32_e32 v33, v45, v247
	v_add_f32_e32 v32, v32, v201
	v_exp_f32_e32 v217, v33
	v_sub_f32_e32 v33, v46, v247
	v_add_f32_e32 v32, v32, v214
	v_exp_f32_e32 v222, v33
	v_sub_f32_e32 v33, v47, v247
	v_add_f32_e32 v32, v32, v215
	v_exp_f32_e32 v223, v33
	v_sub_f32_e32 v16, v16, v247
	v_add_f32_e32 v32, v32, v216
	v_exp_f32_e32 v70, v16
	v_sub_f32_e32 v16, v17, v247
	v_add_f32_e32 v32, v32, v217
	v_exp_f32_e32 v71, v16
	v_sub_f32_e32 v16, v18, v247
	v_add_f32_e32 v32, v32, v222
	v_exp_f32_e32 v76, v16
	v_sub_f32_e32 v16, v19, v247
	v_add_f32_e32 v32, v32, v223
	v_exp_f32_e32 v77, v16
	v_sub_f32_e32 v17, v20, v247
	v_add_f32_e32 v16, v32, v70
	v_exp_f32_e32 v78, v17
	v_sub_f32_e32 v17, v21, v247
	v_add_f32_e32 v16, v16, v71
	v_exp_f32_e32 v79, v17
	v_sub_f32_e32 v17, v22, v247
	v_add_f32_e32 v16, v16, v76
	v_exp_f32_e32 v168, v17
	v_sub_f32_e32 v17, v23, v247
	v_add_f32_e32 v16, v16, v77
	v_exp_f32_e32 v169, v17
	v_sub_f32_e32 v17, v24, v247
	v_add_f32_e32 v16, v16, v78
	v_exp_f32_e32 v126, v17
	v_sub_f32_e32 v17, v25, v247
	v_add_f32_e32 v16, v16, v79
	v_exp_f32_e32 v127, v17
	v_sub_f32_e32 v17, v26, v247
	v_add_f32_e32 v16, v16, v168
	v_exp_f32_e32 v184, v17
	v_sub_f32_e32 v17, v27, v247
	v_add_f32_e32 v16, v16, v169
	v_exp_f32_e32 v185, v17
	v_sub_f32_e32 v17, v28, v247
	v_add_f32_e32 v16, v16, v126
	v_exp_f32_e32 v186, v17
	v_sub_f32_e32 v17, v29, v247
	v_add_f32_e32 v16, v16, v127
	v_exp_f32_e32 v187, v17
	v_sub_f32_e32 v17, v30, v247
	v_add_f32_e32 v16, v16, v184
	v_exp_f32_e32 v198, v17
	v_sub_f32_e32 v17, v31, v247
	v_add_f32_e32 v16, v16, v185
	v_exp_f32_e32 v199, v17
	v_sub_f32_e32 v0, v0, v247
	v_add_f32_e32 v16, v16, v186
	v_exp_f32_e32 v196, v0
	v_sub_f32_e32 v0, v1, v247
	v_add_f32_e32 v16, v16, v187
	v_exp_f32_e32 v197, v0
	v_sub_f32_e32 v0, v2, v247
	v_add_f32_e32 v16, v16, v198
	v_exp_f32_e32 v210, v0
	v_sub_f32_e32 v0, v3, v247
	v_add_f32_e32 v16, v16, v199
	v_exp_f32_e32 v211, v0
	v_sub_f32_e32 v1, v4, v247
	v_add_f32_e32 v0, v16, v196
	v_exp_f32_e32 v212, v1
	v_sub_f32_e32 v1, v5, v247
	v_add_f32_e32 v0, v0, v197
	v_exp_f32_e32 v213, v1
	v_sub_f32_e32 v1, v6, v247
	v_add_f32_e32 v0, v0, v210
	v_exp_f32_e32 v220, v1
	v_sub_f32_e32 v1, v7, v247
	v_add_f32_e32 v0, v0, v211
	v_exp_f32_e32 v221, v1
	v_sub_f32_e32 v1, v8, v247
	v_add_f32_e32 v0, v0, v212
	v_exp_f32_e32 v218, v1
	v_sub_f32_e32 v1, v9, v247
	v_add_f32_e32 v0, v0, v213
	v_exp_f32_e32 v219, v1
	v_sub_f32_e32 v1, v10, v247
	v_add_f32_e32 v0, v0, v220
	v_exp_f32_e32 v224, v1
	v_sub_f32_e32 v1, v11, v247
	v_add_f32_e32 v0, v0, v221
	v_exp_f32_e32 v225, v1
	v_sub_f32_e32 v1, v12, v247
	v_add_f32_e32 v0, v0, v218
	v_exp_f32_e32 v226, v1
	v_sub_f32_e32 v1, v13, v247
	v_add_f32_e32 v0, v0, v219
	v_exp_f32_e32 v227, v1
	v_sub_f32_e32 v1, v14, v247
	v_add_f32_e32 v0, v0, v224
	v_exp_f32_e32 v228, v1
	v_sub_f32_e32 v1, v15, v247
	v_add_f32_e32 v0, v0, v225
	v_exp_f32_e32 v229, v1
	v_add_f32_e32 v0, v0, v226
	v_add_f32_e32 v0, v0, v227
	v_add_f32_e32 v0, v0, v228
	v_add_f32_e32 v0, v0, v229
	ds_bpermute_b32 v1, v234, v0
	s_and_saveexec_b64 s[24:25], s[0:1]
	s_cbranch_execz .LBB1_18
	s_waitcnt lgkmcnt(0)
	v_add_f32_e32 v0, v0, v1
	v_add_u32_e32 v1, s31, v236
	ds_write_b32 v1, v0
